# window attention row sums on 2-pass 4x4x4 bf16 MFMAs as well (two accumulator quads, second one in free registers with its own rescale)
# baseline (speedup 1.0000x reference)
.LBB0_1932:
	v_exp_f32_e32 v50, v50
	v_exp_f32_e32 v66, v66
	v_exp_f32_e32 v51, v51
	v_exp_f32_e32 v67, v67
	v_exp_f32_e32 v52, v52
	v_exp_f32_e32 v68, v68
	v_exp_f32_e32 v53, v53
	v_exp_f32_e32 v69, v69
	v_exp_f32_e32 v54, v54
	v_exp_f32_e32 v70, v70
	v_exp_f32_e32 v55, v55
	v_exp_f32_e32 v71, v71
	v_exp_f32_e32 v56, v56
	v_exp_f32_e32 v72, v72
	v_exp_f32_e32 v57, v57
	v_exp_f32_e32 v73, v73
	v_exp_f32_e32 v58, v58
	v_exp_f32_e32 v74, v74
	v_exp_f32_e32 v59, v59
	v_exp_f32_e32 v75, v75
	v_exp_f32_e32 v60, v60
	v_exp_f32_e32 v76, v76
	v_exp_f32_e32 v61, v61
	v_exp_f32_e32 v77, v77
	v_exp_f32_e32 v62, v62
	v_exp_f32_e32 v78, v78
	v_exp_f32_e32 v63, v63
	v_exp_f32_e32 v79, v79
	v_exp_f32_e32 v64, v64
	v_exp_f32_e32 v80, v80
	v_exp_f32_e32 v65, v65
	v_exp_f32_e32 v81, v81
	v_cvt_pk_bf16_f32 v50, v50, v51
	v_cvt_pk_bf16_f32 v51, v52, v53
	v_cvt_pk_bf16_f32 v52, v54, v55
	v_cvt_pk_bf16_f32 v53, v56, v57
	v_cvt_pk_bf16_f32 v54, v66, v67
	v_cvt_pk_bf16_f32 v55, v68, v69
	v_cvt_pk_bf16_f32 v56, v70, v71
	v_cvt_pk_bf16_f32 v57, v72, v73
	v_cvt_pk_bf16_f32 v58, v58, v59
	v_cvt_pk_bf16_f32 v59, v60, v61
	v_cvt_pk_bf16_f32 v60, v62, v63
	v_cvt_pk_bf16_f32 v61, v64, v65
	v_cvt_pk_bf16_f32 v62, v74, v75
	v_cvt_pk_bf16_f32 v63, v76, v77
	v_cvt_pk_bf16_f32 v64, v78, v79
	v_cvt_pk_bf16_f32 v65, v80, v81
	v_mov_b64_e32 v[66:67], s[92:93]
	v_mov_b64_e32 v[68:69], s[94:95]
	s_not_b32 s2, s85
	s_lshl_b32 s2, s2, 13
	s_and_b32 s2, s2, 0x2000
	s_add_i32 s2, s2, 0
	v_mfma_f32_4x4x4_16b_bf16 v[34:37], v[66:67], v[50:51], v[34:37]
	v_mfma_f32_4x4x4_16b_bf16 v[180:183], v[66:67], v[52:53], v[180:183]
	s_addk_i32 s2, 0x4000
	v_add_u32_e32 v82, s2, v177
	v_add_u32_e32 v83, s2, v178
	ds_read_b64_tr_b16 v[70:71], v82 offset:0
	ds_read_b64_tr_b16 v[72:73], v82 offset:1024
	ds_read_b64_tr_b16 v[74:75], v83 offset:0
	ds_read_b64_tr_b16 v[76:77], v83 offset:1024
	v_mfma_f32_4x4x4_16b_bf16 v[34:37], v[66:67], v[58:59], v[34:37]
	v_mfma_f32_4x4x4_16b_bf16 v[180:183], v[66:67], v[60:61], v[180:183]
	s_nop 0
	v_mfma_f32_4x4x4_16b_bf16 v[34:37], v[66:67], v[54:55], v[34:37]
	v_mfma_f32_4x4x4_16b_bf16 v[180:183], v[66:67], v[56:57], v[180:183]
	s_nop 0
	v_mfma_f32_4x4x4_16b_bf16 v[34:37], v[66:67], v[62:63], v[34:37]
	v_mfma_f32_4x4x4_16b_bf16 v[180:183], v[66:67], v[64:65], v[180:183]
	ds_read_b64_tr_b16 v[66:67], v82 offset:2048
	ds_read_b64_tr_b16 v[68:69], v82 offset:3072
	ds_read_b64_tr_b16 v[78:79], v83 offset:2048
	ds_read_b64_tr_b16 v[80:81], v83 offset:3072
	s_nop 0
	s_waitcnt lgkmcnt(0)
	ds_read_b64_tr_b16 v[36:37], v82 offset:4096
	ds_read_b64_tr_b16 v[38:39], v82 offset:5120
	ds_read_b64_tr_b16 v[40:41], v83 offset:4096
	ds_read_b64_tr_b16 v[42:43], v83 offset:5120
	ds_read_b64_tr_b16 v[44:45], v82 offset:6144
	s_nop 0
	v_mfma_f32_32x32x16_bf16 v[18:33], v[70:73], v[50:53], v[18:33]
	ds_read_b64_tr_b16 v[46:47], v82 offset:7168
	ds_read_b64_tr_b16 v[48:49], v83 offset:6144
	v_mfma_f32_32x32x16_bf16 v[2:17], v[74:77], v[50:53], v[2:17]
	ds_read_b64_tr_b16 v[50:51], v83 offset:7168
	s_nop 0
	s_waitcnt lgkmcnt(0)
	v_mfma_f32_32x32x16_bf16 v[18:33], v[66:69], v[58:61], v[18:33]
	v_mfma_f32_32x32x16_bf16 v[2:17], v[78:81], v[58:61], v[2:17]
	s_nop 4
	v_mfma_f32_32x32x16_bf16 v[18:33], v[36:39], v[54:57], v[18:33]
	v_mfma_f32_32x32x16_bf16 v[2:17], v[40:43], v[54:57], v[2:17]
	v_mfma_f32_32x32x16_bf16 v[18:33], v[44:47], v[62:65], v[18:33]
	v_mfma_f32_32x32x16_bf16 v[2:17], v[48:51], v[62:65], v[2:17]
	s_setprio 0
	v_add_f32_e32 v36, v34, v180
	v_mov_b32_e32 v37, v36
	s_nop 1
	v_permlane32_swap_b32_e32 v36, v37
	v_add_f32_e32 v37, v36, v37
	v_fmac_f32_e32 v175, 0.5, v37
	v_mov_b32_e32 v36, v175
	v_readlane_b32 s2, v255, 30
	s_nop 0
	v_permlane32_swap_b32_e32 v175, v36
	v_lshlrev_b64 v[34:35], 11, v[144:145]
	v_readlane_b32 s3, v255, 31
	v_add_f32_e32 v36, v175, v175
	v_lshlrev_b32_e32 v98, 1, v116
	v_lshl_add_u64 v[34:35], s[2:3], 0, v[34:35]
	v_div_scale_f32 v37, s[2:3], v36, v36, 1.0
	v_rcp_f32_e32 v38, v37
	v_lshl_add_u64 v[34:35], v[146:147], 1, v[34:35]
	v_lshl_add_u64 v[34:35], v[34:35], 0, v[98:99]
	s_addk_i32 s84, 0x100
	v_fma_f32 v39, -v37, v38, 1.0
	v_fmac_f32_e32 v38, v39, v38
	v_div_scale_f32 v39, vcc, 1.0, v36, 1.0
	v_mul_f32_e32 v40, v39, v38
	v_fma_f32 v41, -v37, v40, v39
	v_fmac_f32_e32 v40, v41, v38
	v_fma_f32 v37, -v37, v40, v39
	v_div_fmas_f32 v37, v37, v38, v40
	v_div_fixup_f32 v36, v37, v36, 1.0
	v_pk_mul_f32 v[18:19], v[18:19], v[36:37] op_sel_hi:[1,0]
	v_pk_mul_f32 v[20:21], v[20:21], v[36:37] op_sel_hi:[1,0]
	v_pk_mul_f32 v[2:3], v[2:3], v[36:37] op_sel_hi:[1,0]
	v_pk_mul_f32 v[4:5], v[4:5], v[36:37] op_sel_hi:[1,0]
	v_cvt_pk_bf16_f32 v18, v18, v19
	v_cvt_pk_bf16_f32 v19, v20, v21
	v_pk_mul_f32 v[20:21], v[22:23], v[36:37] op_sel_hi:[1,0]
	v_pk_mul_f32 v[22:23], v[24:25], v[36:37] op_sel_hi:[1,0]
	v_cvt_pk_bf16_f32 v2, v2, v3
	v_cvt_pk_bf16_f32 v3, v4, v5
	v_pk_mul_f32 v[4:5], v[6:7], v[36:37] op_sel_hi:[1,0]
	v_pk_mul_f32 v[6:7], v[8:9], v[36:37] op_sel_hi:[1,0]
	v_cvt_pk_bf16_f32 v20, v20, v21
	v_cvt_pk_bf16_f32 v21, v22, v23
	v_cvt_pk_bf16_f32 v4, v4, v5
	v_cvt_pk_bf16_f32 v5, v6, v7
	v_permlane32_swap_b32_e32 v18, v20
	v_permlane32_swap_b32_e32 v19, v21
	v_permlane32_swap_b32_e32 v2, v4
	v_permlane32_swap_b32_e32 v3, v5
	global_store_dwordx4 v[34:35], v[18:21], off
	global_store_dwordx4 v[34:35], v[2:5], off offset:64
	v_pk_mul_f32 v[22:23], v[32:33], v[36:37] op_sel_hi:[1,0]
	v_pk_mul_f32 v[18:19], v[26:27], v[36:37] op_sel_hi:[1,0]
	v_pk_mul_f32 v[20:21], v[28:29], v[36:37] op_sel_hi:[1,0]
	v_pk_mul_f32 v[2:3], v[10:11], v[36:37] op_sel_hi:[1,0]
	v_pk_mul_f32 v[4:5], v[12:13], v[36:37] op_sel_hi:[1,0]
	v_cvt_pk_bf16_f32 v18, v18, v19
	v_cvt_pk_bf16_f32 v19, v20, v21
	v_pk_mul_f32 v[20:21], v[30:31], v[36:37] op_sel_hi:[1,0]
	v_cvt_pk_bf16_f32 v2, v2, v3
	v_cvt_pk_bf16_f32 v3, v4, v5
	v_pk_mul_f32 v[4:5], v[14:15], v[36:37] op_sel_hi:[1,0]
	v_pk_mul_f32 v[6:7], v[16:17], v[36:37] op_sel_hi:[1,0]
	v_cvt_pk_bf16_f32 v20, v20, v21
	v_cvt_pk_bf16_f32 v21, v22, v23
	v_cvt_pk_bf16_f32 v4, v4, v5
	v_cvt_pk_bf16_f32 v5, v6, v7
	v_permlane32_swap_b32_e32 v18, v20
	v_permlane32_swap_b32_e32 v19, v21
	v_permlane32_swap_b32_e32 v2, v4
	v_permlane32_swap_b32_e32 v3, v5
	s_cmp_ge_u32 s84, s82
	global_store_dwordx4 v[34:35], v[18:21], off offset:32
	global_store_dwordx4 v[34:35], v[2:5], off offset:96
	s_cbranch_scc1 .LBB0_2100

.LBB0_1971:
	v_max3_f32 v2, v50, v51, v66
	s_nop 7
	v_max_f32_e32 v3, v65, v65
	v_max3_f32 v2, v2, v67, v52
	s_nop 0
	v_max3_f32 v2, v2, v68, v69
	s_nop 0
	v_max3_f32 v2, v2, v53, v54
	s_nop 0
	v_max3_f32 v2, v2, v70, v71
	s_nop 0
	v_max3_f32 v2, v2, v55, v56
	s_nop 0
	v_max3_f32 v2, v2, v72, v73
	s_nop 0
	v_max3_f32 v2, v2, v57, v58
	s_nop 0
	v_max3_f32 v2, v2, v74, v75
	s_nop 0
	v_max3_f32 v2, v2, v59, v60
	s_nop 0
	v_max3_f32 v2, v2, v76, v77
	s_nop 0
	v_max3_f32 v2, v2, v61, v62
	s_nop 0
	v_max3_f32 v2, v2, v78, v79
	s_nop 0
	v_max3_f32 v2, v2, v63, v64
	s_nop 0
	v_max3_f32 v2, v2, v80, v81
	s_nop 0
	v_max_f32_e32 v2, v2, v2
	v_max_f32_e32 v120, v2, v3
	v_mov_b32_e32 v2, v120
	s_nop 1
	v_permlane32_swap_b32_e32 v120, v2
	v_cmp_lt_f32_e32 vcc, s29, v120
	s_cbranch_vccz .LBB0_2075
	v_max_f32_e32 v2, v120, v120
	v_max_f32_e32 v89, 0, v2
	v_exp_f32_e64 v90, -v89
	v_add_f32_e32 v184, 0, v89
	v_mul_f32_e32 v18, 0, v90
	v_mov_b32_e32 v19, v18
	v_mov_b32_e32 v20, v18
	v_mov_b32_e32 v21, v18
	v_mov_b32_e32 v22, v18
	v_mov_b32_e32 v23, v18
	v_mov_b32_e32 v24, v18
	v_mov_b32_e32 v25, v18
	v_mov_b32_e32 v26, v18
	v_mov_b32_e32 v27, v18
	v_mov_b32_e32 v28, v18
	v_mov_b32_e32 v29, v18
	v_mov_b32_e32 v30, v18
	v_mov_b32_e32 v31, v18
	v_mov_b32_e32 v32, v18
	v_mov_b32_e32 v33, v18
	v_mov_b32_e32 v2, v18
	v_mov_b32_e32 v3, v18
	v_mov_b32_e32 v4, v18
	v_mov_b32_e32 v5, v18
	v_mov_b32_e32 v6, v18
	v_mov_b32_e32 v7, v18
	v_mov_b32_e32 v8, v18
	v_mov_b32_e32 v9, v18
	v_mov_b32_e32 v10, v18
	v_mov_b32_e32 v11, v18
	v_mov_b32_e32 v12, v18
	v_mov_b32_e32 v13, v18
	v_mov_b32_e32 v14, v18
	v_mov_b32_e32 v15, v18
	v_mov_b32_e32 v16, v18
	v_mov_b32_e32 v17, v18
	v_mov_b32_e32 v34, v18
	v_mov_b32_e32 v180, v18
	v_mov_b32_e32 v35, v18
	v_mov_b32_e32 v36, v18
	v_mov_b32_e32 v37, v18
	v_mov_b32_e32 v38, v18
	v_mov_b32_e32 v39, v18
	v_mov_b32_e32 v40, v18
	v_mov_b32_e32 v41, v18
	v_mov_b32_e32 v42, v18
	v_mov_b32_e32 v43, v18
	v_mov_b32_e32 v44, v18
	v_mov_b32_e32 v45, v18
	v_mov_b32_e32 v46, v18
	v_mov_b32_e32 v47, v18
	v_mov_b32_e32 v48, v18
	v_mov_b32_e32 v49, v18
	v_mul_f32_e32 v175, v175, v90
	v_cmp_neq_f32_e32 vcc, 0, v184
	s_cbranch_vccz .LBB0_1974

.LBB0_2006:
	v_max3_f32 v86, v100, v101, v116
	v_max_f32_e32 v87, v115, v115
	v_max3_f32 v86, v86, v117, v102
	s_nop 0
	v_mfma_f32_4x4x4_16b_bf16 v[34:37], v[240:241], v[58:59], v[34:37]
	v_mfma_f32_4x4x4_16b_bf16 v[180:183], v[240:241], v[60:61], v[180:183]
	v_max3_f32 v86, v86, v118, v119
	v_max3_f32 v86, v86, v103, v104
	v_max3_f32 v86, v86, v120, v121
	v_max3_f32 v86, v86, v105, v106
	v_mfma_f32_4x4x4_16b_bf16 v[34:37], v[240:241], v[62:63], v[34:37]
	v_mfma_f32_4x4x4_16b_bf16 v[180:183], v[240:241], v[64:65], v[180:183]
	v_max3_f32 v86, v86, v122, v123
	v_max3_f32 v86, v86, v107, v108
	v_max3_f32 v86, v86, v124, v125
	v_max3_f32 v86, v86, v109, v110
	v_mfma_f32_4x4x4_16b_bf16 v[34:37], v[240:241], v[54:55], v[34:37]
	v_mfma_f32_4x4x4_16b_bf16 v[180:183], v[240:241], v[56:57], v[180:183]
	v_max3_f32 v86, v86, v126, v127
	v_max3_f32 v86, v86, v111, v112
	v_max3_f32 v86, v86, v128, v129
	v_max3_f32 v86, v86, v113, v114
	v_mfma_f32_4x4x4_16b_bf16 v[34:37], v[240:241], v[50:51], v[34:37]
	v_mfma_f32_4x4x4_16b_bf16 v[180:183], v[240:241], v[52:53], v[180:183]
	v_max3_f32 v86, v86, v130, v131
	v_max_f32_e32 v86, v86, v86
	v_max_f32_e32 v86, v86, v87
	v_mov_b32_e32 v87, v86
	s_nop 1
	v_permlane32_swap_b32_e32 v86, v87
	v_sub_f32_e32 v86, v86, v184
	s_waitcnt lgkmcnt(0)
	s_nop 0
	v_mfma_f32_32x32x16_bf16 v[18:33], v[78:81], v[58:61], v[18:33]
	v_mfma_f32_32x32x16_bf16 v[2:17], v[74:77], v[58:61], v[2:17]
	ds_read_b64_tr_b16 v[58:59], v200 offset:4096
	ds_read_b64_tr_b16 v[60:61], v200 offset:5120
	v_mfma_f32_32x32x16_bf16 v[18:33], v[70:73], v[62:65], v[18:33]
	v_mfma_f32_32x32x16_bf16 v[2:17], v[66:69], v[62:65], v[2:17]
	ds_read_b64_tr_b16 v[62:63], v201 offset:4096
	ds_read_b64_tr_b16 v[64:65], v201 offset:5120
	ds_read_b64_tr_b16 v[66:67], v200 offset:6144
	ds_read_b64_tr_b16 v[68:69], v200 offset:7168
	ds_read_b64_tr_b16 v[70:71], v201 offset:6144
	ds_read_b64_tr_b16 v[72:73], v201 offset:7168
	s_nop 0
	s_waitcnt lgkmcnt(0)
	s_nop 0
	v_mfma_f32_32x32x16_bf16 v[18:33], v[58:61], v[54:57], v[18:33]
	v_mfma_f32_32x32x16_bf16 v[2:17], v[62:65], v[54:57], v[2:17]
	v_mfma_f32_32x32x16_bf16 v[18:33], v[66:69], v[50:53], v[18:33]
	v_mfma_f32_32x32x16_bf16 v[2:17], v[70:73], v[50:53], v[2:17]
	v_cmp_lt_f32_e32 vcc, s29, v86
	s_cbranch_vccz .LBB0_2008
	v_max_f32_e32 v50, v86, v86
	v_max_f32_e32 v51, 0, v50
	v_exp_f32_e64 v50, -v51
	v_add_f32_e32 v184, v184, v51
	v_mul_f32_e32 v175, v175, v50
	v_pk_mul_f32 v[48:49], v[48:49], v[50:51] op_sel_hi:[1,0]
	v_pk_mul_f32 v[46:47], v[46:47], v[50:51] op_sel_hi:[1,0]
	v_pk_mul_f32 v[44:45], v[44:45], v[50:51] op_sel_hi:[1,0]
	v_pk_mul_f32 v[42:43], v[42:43], v[50:51] op_sel_hi:[1,0]
	v_pk_mul_f32 v[40:41], v[40:41], v[50:51] op_sel_hi:[1,0]
	v_pk_mul_f32 v[38:39], v[38:39], v[50:51] op_sel_hi:[1,0]
	v_pk_mul_f32 v[36:37], v[36:37], v[50:51] op_sel_hi:[1,0]
	v_pk_mul_f32 v[34:35], v[34:35], v[50:51] op_sel_hi:[1,0]
	v_pk_mul_f32 v[180:181], v[180:181], v[50:51] op_sel_hi:[1,0]
	v_pk_mul_f32 v[16:17], v[50:51], v[16:17] op_sel_hi:[0,1]
	v_pk_mul_f32 v[14:15], v[50:51], v[14:15] op_sel_hi:[0,1]
	v_pk_mul_f32 v[12:13], v[50:51], v[12:13] op_sel_hi:[0,1]
	v_pk_mul_f32 v[10:11], v[50:51], v[10:11] op_sel_hi:[0,1]
	v_pk_mul_f32 v[8:9], v[50:51], v[8:9] op_sel_hi:[0,1]
	v_pk_mul_f32 v[6:7], v[50:51], v[6:7] op_sel_hi:[0,1]
	v_pk_mul_f32 v[4:5], v[50:51], v[4:5] op_sel_hi:[0,1]
	v_pk_mul_f32 v[2:3], v[50:51], v[2:3] op_sel_hi:[0,1]
	v_pk_mul_f32 v[32:33], v[50:51], v[32:33] op_sel_hi:[0,1]
	v_pk_mul_f32 v[30:31], v[50:51], v[30:31] op_sel_hi:[0,1]
	v_pk_mul_f32 v[28:29], v[50:51], v[28:29] op_sel_hi:[0,1]
	v_pk_mul_f32 v[26:27], v[50:51], v[26:27] op_sel_hi:[0,1]
	v_pk_mul_f32 v[24:25], v[50:51], v[24:25] op_sel_hi:[0,1]
	v_pk_mul_f32 v[22:23], v[50:51], v[22:23] op_sel_hi:[0,1]
	v_pk_mul_f32 v[20:21], v[50:51], v[20:21] op_sel_hi:[0,1]
	v_pk_mul_f32 v[18:19], v[50:51], v[18:19] op_sel_hi:[0,1]

.LBB0_2044:
	v_max3_f32 v98, v50, v51, v66
	v_max_f32_e32 v120, v65, v65
	v_max3_f32 v98, v98, v67, v52
	s_nop 0
	v_mfma_f32_4x4x4_16b_bf16 v[34:37], v[240:241], v[94:95], v[34:37]
	v_mfma_f32_4x4x4_16b_bf16 v[180:183], v[240:241], v[96:97], v[180:183]
	v_max3_f32 v98, v98, v68, v69
	v_max3_f32 v98, v98, v53, v54
	v_max3_f32 v98, v98, v70, v71
	v_max3_f32 v98, v98, v55, v56
	v_mfma_f32_4x4x4_16b_bf16 v[34:37], v[240:241], v[100:101], v[34:37]
	v_mfma_f32_4x4x4_16b_bf16 v[180:183], v[240:241], v[102:103], v[180:183]
	v_max3_f32 v98, v98, v72, v73
	v_max3_f32 v98, v98, v57, v58
	v_max3_f32 v98, v98, v74, v75
	v_max3_f32 v98, v98, v59, v60
	v_mfma_f32_4x4x4_16b_bf16 v[34:37], v[240:241], v[90:91], v[34:37]
	v_mfma_f32_4x4x4_16b_bf16 v[180:183], v[240:241], v[92:93], v[180:183]
	v_max3_f32 v98, v98, v76, v77
	v_max3_f32 v98, v98, v61, v62
	v_max3_f32 v98, v98, v78, v79
	v_max3_f32 v98, v98, v63, v64
	v_mfma_f32_4x4x4_16b_bf16 v[34:37], v[240:241], v[86:87], v[34:37]
	v_mfma_f32_4x4x4_16b_bf16 v[180:183], v[240:241], v[88:89], v[180:183]
	v_max3_f32 v98, v98, v80, v81
	v_max_f32_e32 v98, v98, v98
	v_max_f32_e32 v98, v98, v120
	v_mov_b32_e32 v120, v98
	s_nop 1
	v_permlane32_swap_b32_e32 v98, v120
	v_sub_f32_e32 v120, v98, v184
	s_waitcnt lgkmcnt(0)
	s_nop 0
	v_mfma_f32_32x32x16_bf16 v[18:33], v[116:119], v[94:97], v[18:33]
	v_mfma_f32_32x32x16_bf16 v[2:17], v[112:115], v[94:97], v[2:17]
	ds_read_b64_tr_b16 v[94:95], v202 offset:4096
	ds_read_b64_tr_b16 v[96:97], v202 offset:5120
	v_mfma_f32_32x32x16_bf16 v[18:33], v[108:111], v[100:103], v[18:33]
	v_mfma_f32_32x32x16_bf16 v[2:17], v[104:107], v[100:103], v[2:17]
	ds_read_b64_tr_b16 v[100:101], v203 offset:4096
	ds_read_b64_tr_b16 v[102:103], v203 offset:5120
	ds_read_b64_tr_b16 v[104:105], v202 offset:6144
	ds_read_b64_tr_b16 v[106:107], v202 offset:7168
	ds_read_b64_tr_b16 v[108:109], v203 offset:6144
	ds_read_b64_tr_b16 v[110:111], v203 offset:7168
	s_nop 0
	s_waitcnt lgkmcnt(0)
	s_nop 0
	v_mfma_f32_32x32x16_bf16 v[18:33], v[94:97], v[90:93], v[18:33]
	v_mfma_f32_32x32x16_bf16 v[2:17], v[100:103], v[90:93], v[2:17]
	v_mfma_f32_32x32x16_bf16 v[18:33], v[104:107], v[86:89], v[18:33]
	v_mfma_f32_32x32x16_bf16 v[2:17], v[108:111], v[86:89], v[2:17]
	v_cmp_lt_f32_e32 vcc, s29, v120
	s_cbranch_vccz .LBB0_2046
	v_max_f32_e32 v86, v120, v120
	v_max_f32_e32 v87, 0, v86
	v_exp_f32_e64 v86, -v87
	v_add_f32_e32 v184, v184, v87
	v_mul_f32_e32 v175, v175, v86
	v_pk_mul_f32 v[48:49], v[48:49], v[86:87] op_sel_hi:[1,0]
	v_pk_mul_f32 v[46:47], v[46:47], v[86:87] op_sel_hi:[1,0]
	v_pk_mul_f32 v[44:45], v[44:45], v[86:87] op_sel_hi:[1,0]
	v_pk_mul_f32 v[42:43], v[42:43], v[86:87] op_sel_hi:[1,0]
	v_pk_mul_f32 v[40:41], v[40:41], v[86:87] op_sel_hi:[1,0]
	v_pk_mul_f32 v[38:39], v[38:39], v[86:87] op_sel_hi:[1,0]
	v_pk_mul_f32 v[36:37], v[36:37], v[86:87] op_sel_hi:[1,0]
	v_pk_mul_f32 v[34:35], v[34:35], v[86:87] op_sel_hi:[1,0]
	v_pk_mul_f32 v[180:181], v[180:181], v[86:87] op_sel_hi:[1,0]
	v_pk_mul_f32 v[16:17], v[86:87], v[16:17] op_sel_hi:[0,1]
	v_pk_mul_f32 v[14:15], v[86:87], v[14:15] op_sel_hi:[0,1]
	v_pk_mul_f32 v[12:13], v[86:87], v[12:13] op_sel_hi:[0,1]
	v_pk_mul_f32 v[10:11], v[86:87], v[10:11] op_sel_hi:[0,1]
	v_pk_mul_f32 v[8:9], v[86:87], v[8:9] op_sel_hi:[0,1]
	v_pk_mul_f32 v[6:7], v[86:87], v[6:7] op_sel_hi:[0,1]
	v_pk_mul_f32 v[4:5], v[86:87], v[4:5] op_sel_hi:[0,1]
	v_pk_mul_f32 v[2:3], v[86:87], v[2:3] op_sel_hi:[0,1]
	v_pk_mul_f32 v[32:33], v[86:87], v[32:33] op_sel_hi:[0,1]
	v_pk_mul_f32 v[30:31], v[86:87], v[30:31] op_sel_hi:[0,1]
	v_pk_mul_f32 v[28:29], v[86:87], v[28:29] op_sel_hi:[0,1]
	v_pk_mul_f32 v[26:27], v[86:87], v[26:27] op_sel_hi:[0,1]
	v_pk_mul_f32 v[24:25], v[86:87], v[24:25] op_sel_hi:[0,1]
	v_pk_mul_f32 v[22:23], v[86:87], v[22:23] op_sel_hi:[0,1]
	v_pk_mul_f32 v[20:21], v[86:87], v[20:21] op_sel_hi:[0,1]
	v_pk_mul_f32 v[18:19], v[86:87], v[18:19] op_sel_hi:[0,1]

.LBB0_2075:
	v_mov_b32_e32 v96, v99
	v_mov_b32_e32 v97, v99
	v_mov_b32_e32 v98, v99
	v_mov_b32_e32 v100, v99
	v_mov_b32_e32 v101, v99
	v_mov_b32_e32 v102, v99
	v_mov_b32_e32 v103, v99
	v_mov_b32_e32 v104, v99
	v_mov_b32_e32 v105, v99
	v_mov_b32_e32 v106, v99
	v_mov_b32_e32 v107, v99
	v_mov_b32_e32 v108, v99
	v_mov_b32_e32 v109, v99
	v_mov_b32_e32 v110, v99
	v_mov_b32_e32 v111, v99
	v_mov_b64_e32 v[34:35], v[96:97]
	v_mov_b32_e32 v180, v96
	v_mov_b32_e32 v18, v99
	v_mov_b32_e32 v19, v99
	v_mov_b32_e32 v20, v99
	v_mov_b32_e32 v21, v99
	v_mov_b32_e32 v22, v99
	v_mov_b32_e32 v23, v99
	v_mov_b32_e32 v24, v99
	v_mov_b32_e32 v25, v99
	v_mov_b32_e32 v26, v99
	v_mov_b32_e32 v27, v99
	v_mov_b32_e32 v28, v99
	v_mov_b32_e32 v29, v99
	v_mov_b32_e32 v30, v99
	v_mov_b32_e32 v31, v99
	v_mov_b32_e32 v32, v99
	v_mov_b32_e32 v33, v99
	v_mov_b32_e32 v2, v99
	v_mov_b32_e32 v3, v99
	v_mov_b32_e32 v4, v99
	v_mov_b32_e32 v5, v99
	v_mov_b32_e32 v6, v99
	v_mov_b32_e32 v7, v99
	v_mov_b32_e32 v8, v99
	v_mov_b32_e32 v9, v99
	v_mov_b32_e32 v10, v99
	v_mov_b32_e32 v11, v99
	v_mov_b32_e32 v12, v99
	v_mov_b32_e32 v13, v99
	v_mov_b32_e32 v14, v99
	v_mov_b32_e32 v15, v99
	v_mov_b32_e32 v16, v99
	v_mov_b32_e32 v17, v99
	v_mov_b32_e32 v184, 0
	v_mov_b64_e32 v[36:37], v[98:99]
	v_mov_b64_e32 v[38:39], v[100:101]
	v_mov_b64_e32 v[40:41], v[102:103]
	v_mov_b64_e32 v[42:43], v[104:105]
	v_mov_b64_e32 v[44:45], v[106:107]
	v_mov_b64_e32 v[46:47], v[108:109]
	v_mov_b64_e32 v[48:49], v[110:111]
	v_cmp_neq_f32_e32 vcc, 0, v184
	s_cbranch_vccnz .LBB0_1973
	s_branch .LBB0_1974

.LBB0_2087:
	v_mov_b64_e32 v[124:125], s[94:95]
	v_mov_b64_e32 v[122:123], s[92:93]
	v_max3_f32 v118, v50, v51, v66
	v_max_f32_e32 v119, v65, v65
	v_max3_f32 v118, v118, v67, v52
	s_nop 0
	v_mfma_f32_4x4x4_16b_bf16 v[34:37], v[122:123], v[108:109], v[34:37]
	v_mfma_f32_4x4x4_16b_bf16 v[180:183], v[122:123], v[110:111], v[180:183]
	v_max3_f32 v118, v118, v68, v69
	s_nop 0
	v_max3_f32 v118, v118, v53, v54
	s_nop 0
	v_max3_f32 v118, v118, v70, v71
	s_nop 0
	v_max3_f32 v118, v118, v55, v56
	v_mfma_f32_4x4x4_16b_bf16 v[34:37], v[122:123], v[112:113], v[34:37]
	v_mfma_f32_4x4x4_16b_bf16 v[180:183], v[122:123], v[114:115], v[180:183]
	v_max3_f32 v118, v118, v72, v73
	s_nop 0
	v_max3_f32 v118, v118, v57, v58
	s_nop 0
	v_max3_f32 v118, v118, v74, v75
	s_nop 0
	v_max3_f32 v118, v118, v59, v60
	v_mfma_f32_4x4x4_16b_bf16 v[34:37], v[122:123], v[104:105], v[34:37]
	v_mfma_f32_4x4x4_16b_bf16 v[180:183], v[122:123], v[106:107], v[180:183]
	v_max3_f32 v118, v118, v76, v77
	s_nop 0
	v_max3_f32 v118, v118, v61, v62
	s_nop 0
	v_max3_f32 v118, v118, v78, v79
	s_nop 0
	v_max3_f32 v118, v118, v63, v64
	v_mfma_f32_4x4x4_16b_bf16 v[34:37], v[122:123], v[100:101], v[34:37]
	v_mfma_f32_4x4x4_16b_bf16 v[180:183], v[122:123], v[102:103], v[180:183]
	v_max3_f32 v118, v118, v80, v81
	s_nop 0
	v_max_f32_e32 v118, v118, v118
	v_max_f32_e32 v118, v118, v119
	v_mov_b32_e32 v119, v118
	s_nop 1
	v_permlane32_swap_b32_e32 v118, v119
	v_sub_f32_e32 v120, v118, v184
	s_waitcnt lgkmcnt(0)
	s_nop 0
	v_mfma_f32_32x32x16_bf16 v[18:33], v[94:97], v[108:111], v[18:33]
	v_mfma_f32_32x32x16_bf16 v[2:17], v[90:93], v[108:111], v[2:17]
	v_mfma_f32_32x32x16_bf16 v[18:33], v[86:89], v[112:115], v[18:33]
	v_mfma_f32_32x32x16_bf16 v[2:17], v[82:85], v[112:115], v[2:17]
	ds_read_b64_tr_b16 v[82:83], v117 offset:4096
	ds_read_b64_tr_b16 v[84:85], v117 offset:5120
	ds_read_b64_tr_b16 v[86:87], v98 offset:4096
	ds_read_b64_tr_b16 v[88:89], v98 offset:5120
	ds_read_b64_tr_b16 v[90:91], v117 offset:6144
	ds_read_b64_tr_b16 v[92:93], v117 offset:7168
	ds_read_b64_tr_b16 v[94:95], v98 offset:6144
	ds_read_b64_tr_b16 v[96:97], v98 offset:7168
	s_nop 0
	s_waitcnt lgkmcnt(0)
	s_nop 0
	v_mfma_f32_32x32x16_bf16 v[18:33], v[82:85], v[104:107], v[18:33]
	v_mfma_f32_32x32x16_bf16 v[2:17], v[86:89], v[104:107], v[2:17]
	v_mfma_f32_32x32x16_bf16 v[18:33], v[90:93], v[100:103], v[18:33]
	v_mfma_f32_32x32x16_bf16 v[2:17], v[94:97], v[100:103], v[2:17]
	v_cmp_lt_f32_e32 vcc, s29, v120
	s_cbranch_vccz .LBB0_2089
	v_max_f32_e32 v82, v120, v120
	v_max_f32_e32 v83, 0, v82
	v_exp_f32_e64 v82, -v83
	v_add_f32_e32 v184, v184, v83
	v_mul_f32_e32 v175, v175, v82
	v_pk_mul_f32 v[48:49], v[48:49], v[82:83] op_sel_hi:[1,0]
	v_pk_mul_f32 v[46:47], v[46:47], v[82:83] op_sel_hi:[1,0]
	v_pk_mul_f32 v[44:45], v[44:45], v[82:83] op_sel_hi:[1,0]
	v_pk_mul_f32 v[42:43], v[42:43], v[82:83] op_sel_hi:[1,0]
	v_pk_mul_f32 v[40:41], v[40:41], v[82:83] op_sel_hi:[1,0]
	v_pk_mul_f32 v[38:39], v[38:39], v[82:83] op_sel_hi:[1,0]
	v_pk_mul_f32 v[36:37], v[36:37], v[82:83] op_sel_hi:[1,0]
	v_pk_mul_f32 v[34:35], v[34:35], v[82:83] op_sel_hi:[1,0]
	v_pk_mul_f32 v[180:181], v[180:181], v[82:83] op_sel_hi:[1,0]
	v_pk_mul_f32 v[16:17], v[82:83], v[16:17] op_sel_hi:[0,1]
	v_pk_mul_f32 v[14:15], v[82:83], v[14:15] op_sel_hi:[0,1]
	v_pk_mul_f32 v[12:13], v[82:83], v[12:13] op_sel_hi:[0,1]
	v_pk_mul_f32 v[10:11], v[82:83], v[10:11] op_sel_hi:[0,1]
	v_pk_mul_f32 v[8:9], v[82:83], v[8:9] op_sel_hi:[0,1]
	v_pk_mul_f32 v[6:7], v[82:83], v[6:7] op_sel_hi:[0,1]
	v_pk_mul_f32 v[4:5], v[82:83], v[4:5] op_sel_hi:[0,1]
	v_pk_mul_f32 v[2:3], v[82:83], v[2:3] op_sel_hi:[0,1]
	v_pk_mul_f32 v[32:33], v[82:83], v[32:33] op_sel_hi:[0,1]
	v_pk_mul_f32 v[30:31], v[82:83], v[30:31] op_sel_hi:[0,1]
	v_pk_mul_f32 v[28:29], v[82:83], v[28:29] op_sel_hi:[0,1]
	v_pk_mul_f32 v[26:27], v[82:83], v[26:27] op_sel_hi:[0,1]
	v_pk_mul_f32 v[24:25], v[82:83], v[24:25] op_sel_hi:[0,1]
	v_pk_mul_f32 v[22:23], v[82:83], v[22:23] op_sel_hi:[0,1]
	v_pk_mul_f32 v[20:21], v[82:83], v[20:21] op_sel_hi:[0,1]
	v_pk_mul_f32 v[18:19], v[82:83], v[18:19] op_sel_hi:[0,1]
